# speedup vs baseline: 1.0033x; 1.0020x over previous
.Ldn_loop:
	v_add_u32_e32 v147, s17, v146
	v_add_u32_e32 v148, s17, v82
	ds_read_b128 v[118:121], v147 offset:1024
	ds_read_b128 v[134:137], v148 offset:17408
	ds_read_b128 v[138:141], v148 offset:19456
	ds_read_b128 v[142:145], v148 offset:21504
	ds_read_b128 v[122:125], v147 offset:3072
	ds_read_b128 v[126:129], v147 offset:5120
	ds_read_b128 v[130:133], v147 offset:7168
	s_waitcnt lgkmcnt(12)
	v_mfma_f32_16x16x32_f16 v[22:25], v[90:93], v[106:109], v[22:25]
	s_waitcnt lgkmcnt(11)
	v_mfma_f32_16x16x32_f16 v[50:53], v[90:93], v[110:113], v[50:53]
	s_waitcnt lgkmcnt(10)
	v_mfma_f32_16x16x32_f16 v[54:57], v[90:93], v[114:117], v[54:57]
	s_waitcnt lgkmcnt(9)
	v_mfma_f32_16x16x32_f16 v[58:61], v[94:97], v[106:109], v[58:61]
	v_mfma_f32_16x16x32_f16 v[66:69], v[94:97], v[110:113], v[66:69]
	v_mfma_f32_16x16x32_f16 v[62:65], v[94:97], v[114:117], v[62:65]
	s_waitcnt lgkmcnt(8)
	v_mfma_f32_16x16x32_f16 v[42:45], v[98:101], v[106:109], v[42:45]
	v_mfma_f32_16x16x32_f16 v[46:49], v[98:101], v[110:113], v[46:49]
	v_mfma_f32_16x16x32_f16 v[30:33], v[98:101], v[114:117], v[30:33]
	s_waitcnt lgkmcnt(7)
	v_mfma_f32_16x16x32_f16 v[34:37], v[102:105], v[106:109], v[34:37]
	v_mfma_f32_16x16x32_f16 v[38:41], v[102:105], v[110:113], v[38:41]
	v_mfma_f32_16x16x32_f16 v[26:29], v[102:105], v[114:117], v[26:29]
	s_waitcnt vmcnt(5) lgkmcnt(0)
	s_barrier
	v_add_u32_e32 v147, s18, v146
	v_add_u32_e32 v148, s18, v82
	ds_read_b128 v[90:93], v147
	ds_read_b128 v[106:109], v148 offset:16384
	ds_read_b128 v[110:113], v148 offset:18432
	ds_read_b128 v[114:117], v148 offset:20480
	ds_read_b128 v[94:97], v147 offset:2048
	ds_read_b128 v[98:101], v147 offset:4096
	ds_read_b128 v[102:105], v147 offset:6144
	s_add_u32 s6, s17, s16
	s_mov_b32 m0, s6
	v_lshl_add_u64 v[2:3], v[78:79], 0, s[4:5]
	global_load_lds_dwordx4 v[2:3], off
	v_mfma_f32_16x16x32_f16 v[22:25], v[118:121], v[134:137], v[22:25]
	v_mfma_f32_16x16x32_f16 v[50:53], v[118:121], v[138:141], v[50:53]
	v_mfma_f32_16x16x32_f16 v[54:57], v[118:121], v[142:145], v[54:57]
	s_add_u32 m0, s6, 8192
	v_lshl_add_u64 v[4:5], v[76:77], 0, s[4:5]
	global_load_lds_dwordx4 v[4:5], off
	v_mfma_f32_16x16x32_f16 v[58:61], v[122:125], v[134:137], v[58:61]
	v_mfma_f32_16x16x32_f16 v[66:69], v[122:125], v[138:141], v[66:69]
	v_mfma_f32_16x16x32_f16 v[62:65], v[122:125], v[142:145], v[62:65]
	s_add_u32 m0, s6, 16384
	v_lshl_add_u64 v[6:7], v[74:75], 0, s[4:5]
	global_load_lds_dwordx4 v[6:7], off
	v_mfma_f32_16x16x32_f16 v[42:45], v[126:129], v[134:137], v[42:45]
	v_mfma_f32_16x16x32_f16 v[46:49], v[126:129], v[138:141], v[46:49]
	v_mfma_f32_16x16x32_f16 v[30:33], v[126:129], v[142:145], v[30:33]
	s_add_u32 m0, s6, 24576
	v_lshl_add_u64 v[8:9], v[72:73], 0, s[4:5]
	global_load_lds_dwordx4 v[8:9], off
	v_mfma_f32_16x16x32_f16 v[34:37], v[130:133], v[134:137], v[34:37]
	s_add_u32 m0, s6, 32768
	v_lshl_add_u64 v[10:11], v[70:71], 0, s[4:5]
	global_load_lds_dwordx4 v[10:11], off
	v_mfma_f32_16x16x32_f16 v[38:41], v[130:133], v[138:141], v[38:41]
	v_mfma_f32_16x16x32_f16 v[26:29], v[130:133], v[142:145], v[26:29]
	s_add_u32 s4, s4, 0x80
	s_addc_u32 s5, s5, 0
	s_cmpk_eq_i32 s4, 0xf00
	s_mov_b32 s20, s17
	s_mov_b32 s17, s18
	s_mov_b32 s18, s19
	s_mov_b32 s19, s20
	s_cbranch_scc0 .Ldn_loop
	v_add_u32_e32 v147, s17, v146
	v_add_u32_e32 v148, s17, v82
	ds_read_b128 v[118:121], v147 offset:1024
	ds_read_b128 v[134:137], v148 offset:17408
	ds_read_b128 v[138:141], v148 offset:19456
	ds_read_b128 v[142:145], v148 offset:21504
	ds_read_b128 v[122:125], v147 offset:3072
	ds_read_b128 v[126:129], v147 offset:5120
	ds_read_b128 v[130:133], v147 offset:7168
	s_waitcnt lgkmcnt(12)
	v_mfma_f32_16x16x32_f16 v[22:25], v[90:93], v[106:109], v[22:25]
	s_waitcnt lgkmcnt(11)
	v_mfma_f32_16x16x32_f16 v[50:53], v[90:93], v[110:113], v[50:53]
	s_waitcnt lgkmcnt(10)
	v_mfma_f32_16x16x32_f16 v[54:57], v[90:93], v[114:117], v[54:57]
	s_waitcnt lgkmcnt(9)
	v_mfma_f32_16x16x32_f16 v[58:61], v[94:97], v[106:109], v[58:61]
	v_mfma_f32_16x16x32_f16 v[66:69], v[94:97], v[110:113], v[66:69]
	v_mfma_f32_16x16x32_f16 v[62:65], v[94:97], v[114:117], v[62:65]
	s_waitcnt lgkmcnt(8)
	v_mfma_f32_16x16x32_f16 v[42:45], v[98:101], v[106:109], v[42:45]
	v_mfma_f32_16x16x32_f16 v[46:49], v[98:101], v[110:113], v[46:49]
	v_mfma_f32_16x16x32_f16 v[30:33], v[98:101], v[114:117], v[30:33]
	s_waitcnt lgkmcnt(7)
	v_mfma_f32_16x16x32_f16 v[34:37], v[102:105], v[106:109], v[34:37]
	v_mfma_f32_16x16x32_f16 v[38:41], v[102:105], v[110:113], v[38:41]
	v_mfma_f32_16x16x32_f16 v[26:29], v[102:105], v[114:117], v[26:29]
	s_waitcnt vmcnt(5) lgkmcnt(0)
	s_barrier
	v_add_u32_e32 v147, s18, v146
	v_add_u32_e32 v148, s18, v82
	ds_read_b128 v[90:93], v147
	ds_read_b128 v[106:109], v148 offset:16384
	ds_read_b128 v[110:113], v148 offset:18432
	ds_read_b128 v[114:117], v148 offset:20480
	ds_read_b128 v[94:97], v147 offset:2048
	ds_read_b128 v[98:101], v147 offset:4096
	ds_read_b128 v[102:105], v147 offset:6144
	v_mfma_f32_16x16x32_f16 v[22:25], v[118:121], v[134:137], v[22:25]
	v_mfma_f32_16x16x32_f16 v[50:53], v[118:121], v[138:141], v[50:53]
	v_mfma_f32_16x16x32_f16 v[54:57], v[118:121], v[142:145], v[54:57]
	v_mfma_f32_16x16x32_f16 v[58:61], v[122:125], v[134:137], v[58:61]
	v_mfma_f32_16x16x32_f16 v[66:69], v[122:125], v[138:141], v[66:69]
	v_mfma_f32_16x16x32_f16 v[62:65], v[122:125], v[142:145], v[62:65]
	v_mfma_f32_16x16x32_f16 v[42:45], v[126:129], v[134:137], v[42:45]
	v_mfma_f32_16x16x32_f16 v[46:49], v[126:129], v[138:141], v[46:49]
	v_mfma_f32_16x16x32_f16 v[30:33], v[126:129], v[142:145], v[30:33]
	v_mfma_f32_16x16x32_f16 v[34:37], v[130:133], v[134:137], v[34:37]
	v_mfma_f32_16x16x32_f16 v[38:41], v[130:133], v[138:141], v[38:41]
	v_mfma_f32_16x16x32_f16 v[26:29], v[130:133], v[142:145], v[26:29]
	v_add_u32_e32 v78, v87, v88
	ds_read_b128 v[70:73], v78 offset:2048
	ds_read_b128 v[74:77], v78 offset:4096
	ds_read_b128 v[86:89], v78 offset:6144
	ds_read_b128 v[90:93], v82 offset:16384
	ds_read_b128 v[94:97], v82 offset:18432
	ds_read_b128 v[98:101], v78
	ds_read_b128 v[102:105], v82 offset:20480
	s_waitcnt lgkmcnt(1)
	v_mfma_f32_16x16x32_f16 v[22:25], v[98:101], v[90:93], v[22:25]
	v_mfma_f32_16x16x32_f16 v[50:53], v[98:101], v[94:97], v[50:53]
	s_waitcnt lgkmcnt(0)
	v_mfma_f32_16x16x32_f16 v[18:21], v[98:101], v[102:105], v[54:57]
	v_mfma_f32_16x16x32_f16 v[54:57], v[70:73], v[90:93], v[58:61]
	v_mfma_f32_16x16x32_f16 v[58:61], v[70:73], v[94:97], v[66:69]
	v_mfma_f32_16x16x32_f16 v[14:17], v[70:73], v[102:105], v[62:65]
	s_nop 2
	ds_read_b128 v[62:65], v78 offset:3072
	ds_read_b128 v[66:69], v78 offset:5120
	ds_read_b128 v[70:73], v78 offset:7168
	ds_read_b128 v[98:101], v82 offset:17408
	ds_read_b128 v[106:109], v82 offset:19456
	ds_read_b128 v[110:113], v78 offset:1024
	ds_read_b128 v[114:117], v82 offset:21504
	v_mfma_f32_16x16x32_f16 v[42:45], v[74:77], v[90:93], v[42:45]
	s_mov_b32 s3, 0xe000
	v_mfma_f32_16x16x32_f16 v[46:49], v[74:77], v[94:97], v[46:49]
	v_mfma_f32_16x16x32_f16 v[10:13], v[74:77], v[102:105], v[30:33]
	v_mfma_f32_16x16x32_f16 v[30:33], v[86:89], v[90:93], v[34:37]
	v_mfma_f32_16x16x32_f16 v[34:37], v[86:89], v[94:97], v[38:41]
	v_mfma_f32_16x16x32_f16 v[6:9], v[86:89], v[102:105], v[26:29]
	s_waitcnt lgkmcnt(1)
	v_mfma_f32_16x16x32_f16 v[22:25], v[110:113], v[98:101], v[22:25]
	v_mfma_f32_16x16x32_f16 v[26:29], v[110:113], v[106:109], v[50:53]
	s_waitcnt lgkmcnt(0)
	v_mfma_f32_16x16x32_f16 v[2:5], v[110:113], v[114:117], v[18:21]
	v_mfma_f32_16x16x32_f16 v[18:21], v[62:65], v[98:101], v[54:57]
	v_mfma_f32_16x16x32_f16 v[38:41], v[62:65], v[106:109], v[58:61]
	v_mfma_f32_16x16x32_f16 v[14:17], v[62:65], v[114:117], v[14:17]
	v_mfma_f32_16x16x32_f16 v[42:45], v[66:69], v[98:101], v[42:45]
	v_mfma_f32_16x16x32_f16 v[46:49], v[66:69], v[106:109], v[46:49]
	v_mfma_f32_16x16x32_f16 v[10:13], v[66:69], v[114:117], v[10:13]
	v_mfma_f32_16x16x32_f16 v[30:33], v[70:73], v[98:101], v[30:33]
	v_mfma_f32_16x16x32_f16 v[34:37], v[70:73], v[106:109], v[34:37]
	v_mfma_f32_16x16x32_f16 v[6:9], v[70:73], v[114:117], v[6:9]
	s_waitcnt vmcnt(0) lgkmcnt(0)
	s_barrier
	ds_read_b128 v[50:53], v78 offset:43008
	ds_read_b128 v[54:57], v78 offset:45056
	ds_read_b128 v[58:61], v78 offset:47104
	ds_read_b128 v[62:65], v82 offset:57344
	ds_read_b128 v[66:69], v82 offset:59392
	ds_read_b128 v[70:73], v78 offset:40960
	ds_read_b128 v[74:77], v82 offset:61440
	s_waitcnt lgkmcnt(1)
	v_mfma_f32_16x16x32_f16 v[22:25], v[70:73], v[62:65], v[22:25]
	v_mfma_f32_16x16x32_f16 v[26:29], v[70:73], v[66:69], v[26:29]
	s_waitcnt lgkmcnt(0)
	v_mfma_f32_16x16x32_f16 v[2:5], v[70:73], v[74:77], v[2:5]
	v_mfma_f32_16x16x32_f16 v[18:21], v[50:53], v[62:65], v[18:21]
	v_mfma_f32_16x16x32_f16 v[38:41], v[50:53], v[66:69], v[38:41]
	v_mfma_f32_16x16x32_f16 v[14:17], v[50:53], v[74:77], v[14:17]
	ds_read_b128 v[50:53], v78 offset:44032
	ds_read_b128 v[70:73], v78 offset:46080
	ds_read_b128 v[84:87], v78 offset:48128
	ds_read_b128 v[88:91], v82 offset:58368
	ds_read_b128 v[92:95], v82 offset:60416
	ds_read_b128 v[96:99], v78 offset:41984
	ds_read_b128 v[100:103], v82 offset:62464
	v_mfma_f32_16x16x32_f16 v[42:45], v[54:57], v[62:65], v[42:45]
	v_mfma_f32_16x16x32_f16 v[46:49], v[54:57], v[66:69], v[46:49]
	v_mfma_f32_16x16x32_f16 v[10:13], v[54:57], v[74:77], v[10:13]
	v_mfma_f32_16x16x32_f16 v[30:33], v[58:61], v[62:65], v[30:33]
	v_mfma_f32_16x16x32_f16 v[34:37], v[58:61], v[66:69], v[34:37]
	v_mfma_f32_16x16x32_f16 v[6:9], v[58:61], v[74:77], v[6:9]
	s_waitcnt lgkmcnt(1)
	v_mfma_f32_16x16x32_f16 v[22:25], v[96:99], v[88:91], v[22:25]
	v_mfma_f32_16x16x32_f16 v[26:29], v[96:99], v[92:95], v[26:29]
	s_waitcnt lgkmcnt(0)
	v_mfma_f32_16x16x32_f16 v[2:5], v[96:99], v[100:103], v[2:5]
	v_mfma_f32_16x16x32_f16 v[18:21], v[50:53], v[88:91], v[18:21]
	v_mfma_f32_16x16x32_f16 v[38:41], v[50:53], v[92:95], v[38:41]
	v_mfma_f32_16x16x32_f16 v[14:17], v[50:53], v[100:103], v[14:17]
	v_mfma_f32_16x16x32_f16 v[42:45], v[70:73], v[88:91], v[42:45]
	v_mfma_f32_16x16x32_f16 v[46:49], v[70:73], v[92:95], v[46:49]
	v_mfma_f32_16x16x32_f16 v[10:13], v[70:73], v[100:103], v[10:13]
	v_mfma_f32_16x16x32_f16 v[30:33], v[84:87], v[88:91], v[30:33]
	v_mfma_f32_16x16x32_f16 v[34:37], v[84:87], v[92:95], v[34:37]
	v_mfma_f32_16x16x32_f16 v[6:9], v[84:87], v[100:103], v[6:9]
	v_and_or_b32 v50, v80, 12, v81
	v_add_u32_e32 v50, s2, v50
	v_mul_u32_u24_e32 v1, 48, v1
	v_and_or_b32 v52, v0, 15, v1
	v_mul_u32_u24_e32 v0, 0xc00, v50
	v_mov_b32_e32 v1, 0
	v_lshl_add_u64 v[50:51], s[0:1], 0, v[0:1]
	v_add_lshl_u32 v0, v52, s8, 2
	v_lshl_add_u64 v[0:1], v[50:51], 0, v[0:1]
	s_mov_b64 s[0:1], 0x1800
	s_barrier
	global_store_dword v[0:1], v22, off
	global_store_dword v[0:1], v26, off offset:64
	global_store_dword v[0:1], v2, off offset:128
	global_store_dword v[0:1], v23, off offset:3072
	global_store_dword v[0:1], v27, off offset:3136
	global_store_dword v[0:1], v3, off offset:3200
	v_lshl_add_u64 v[2:3], v[0:1], 0, s[0:1]
	s_movk_i32 s0, 0x1000
	v_add_co_u32_e32 v22, vcc, s0, v0
	s_mov_b64 s[0:1], 0x2400
	s_nop 0
	v_addc_co_u32_e32 v23, vcc, 0, v1, vcc
	global_store_dword v[22:23], v24, off offset:2048
	global_store_dword v[2:3], v28, off offset:64
	global_store_dword v[2:3], v4, off offset:128
	v_lshl_add_u64 v[2:3], v[0:1], 0, s[0:1]
	s_movk_i32 s0, 0x2000
	v_add_co_u32_e32 v22, vcc, s0, v0
	s_mov_b64 s[0:1], 0xc000
	s_nop 0
	v_addc_co_u32_e32 v23, vcc, 0, v1, vcc
	global_store_dword v[22:23], v25, off offset:1024
	global_store_dword v[2:3], v29, off offset:64
	global_store_dword v[2:3], v5, off offset:128
	v_lshl_add_u64 v[2:3], v[0:1], 0, s[0:1]
	s_mov_b32 s0, 0xc000
	v_add_co_u32_e32 v4, vcc, s0, v0
	s_mov_b64 s[0:1], 0xcc00
	s_nop 0
	v_addc_co_u32_e32 v5, vcc, 0, v1, vcc
	global_store_dword v[4:5], v18, off
	global_store_dword v[2:3], v38, off offset:64
	global_store_dword v[2:3], v14, off offset:128
	v_lshl_add_u64 v[2:3], v[0:1], 0, s[0:1]
	s_mov_b64 s[0:1], 0xd800
	global_store_dword v[4:5], v19, off offset:3072
	global_store_dword v[2:3], v39, off offset:64
	global_store_dword v[2:3], v15, off offset:128
	v_lshl_add_u64 v[2:3], v[0:1], 0, s[0:1]
	s_mov_b32 s0, 0xd000
	v_add_co_u32_e32 v4, vcc, s0, v0
	s_mov_b64 s[0:1], 0xe400
	s_nop 0
	v_addc_co_u32_e32 v5, vcc, 0, v1, vcc
	global_store_dword v[4:5], v20, off offset:2048
	global_store_dword v[2:3], v40, off offset:64
	global_store_dword v[2:3], v16, off offset:128
	v_add_co_u32_e32 v4, vcc, s3, v0
	v_lshl_add_u64 v[2:3], v[0:1], 0, s[0:1]
	s_nop 0
	v_addc_co_u32_e32 v5, vcc, 0, v1, vcc
	s_mov_b64 s[0:1], 0x18000
	global_store_dword v[4:5], v21, off offset:1024
	global_store_dword v[2:3], v41, off offset:64
	global_store_dword v[2:3], v17, off offset:128
	v_lshl_add_u64 v[2:3], v[0:1], 0, s[0:1]
	s_mov_b32 s0, 0x18000
	v_add_co_u32_e32 v4, vcc, s0, v0
	s_mov_b64 s[0:1], 0x18c00
	s_nop 0
	v_addc_co_u32_e32 v5, vcc, 0, v1, vcc
	global_store_dword v[4:5], v42, off
	global_store_dword v[2:3], v46, off offset:64
	global_store_dword v[2:3], v10, off offset:128
	v_lshl_add_u64 v[2:3], v[0:1], 0, s[0:1]
	s_mov_b64 s[0:1], 0x19800
	global_store_dword v[4:5], v43, off offset:3072
	global_store_dword v[2:3], v47, off offset:64
	global_store_dword v[2:3], v11, off offset:128
	v_lshl_add_u64 v[2:3], v[0:1], 0, s[0:1]
	s_mov_b32 s0, 0x19000
	v_add_co_u32_e32 v4, vcc, s0, v0
	s_mov_b64 s[0:1], 0x1a400
	s_nop 0
	v_addc_co_u32_e32 v5, vcc, 0, v1, vcc
	global_store_dword v[4:5], v44, off offset:2048
	global_store_dword v[2:3], v48, off offset:64
	global_store_dword v[2:3], v12, off offset:128
	v_lshl_add_u64 v[2:3], v[0:1], 0, s[0:1]
	s_mov_b32 s0, 0x1a000
	v_add_co_u32_e32 v4, vcc, s0, v0
	s_mov_b64 s[0:1], 0x24000
	s_nop 0
	v_addc_co_u32_e32 v5, vcc, 0, v1, vcc
	global_store_dword v[4:5], v45, off offset:1024
	global_store_dword v[2:3], v49, off offset:64
	global_store_dword v[2:3], v13, off offset:128
	v_lshl_add_u64 v[2:3], v[0:1], 0, s[0:1]
	s_mov_b32 s0, 0x24000
	v_add_co_u32_e32 v4, vcc, s0, v0
	s_mov_b64 s[0:1], 0x24c00
	s_nop 0
	v_addc_co_u32_e32 v5, vcc, 0, v1, vcc
	global_store_dword v[4:5], v30, off
	global_store_dword v[2:3], v34, off offset:64
	global_store_dword v[2:3], v6, off offset:128
	v_lshl_add_u64 v[2:3], v[0:1], 0, s[0:1]
	s_mov_b64 s[0:1], 0x25800
	global_store_dword v[4:5], v31, off offset:3072
	global_store_dword v[2:3], v35, off offset:64
	global_store_dword v[2:3], v7, off offset:128
	v_lshl_add_u64 v[2:3], v[0:1], 0, s[0:1]
	s_mov_b32 s0, 0x25000
	v_add_co_u32_e32 v4, vcc, s0, v0
	s_mov_b64 s[0:1], 0x26400
	s_nop 0
	v_addc_co_u32_e32 v5, vcc, 0, v1, vcc
	global_store_dword v[4:5], v32, off offset:2048
	global_store_dword v[2:3], v36, off offset:64
	global_store_dword v[2:3], v8, off offset:128
	v_lshl_add_u64 v[2:3], v[0:1], 0, s[0:1]
	v_add_co_u32_e32 v0, vcc, 0x26000, v0
	s_nop 1
	v_addc_co_u32_e32 v1, vcc, 0, v1, vcc
	global_store_dword v[0:1], v33, off offset:1024
	global_store_dword v[2:3], v37, off offset:64
	global_store_dword v[2:3], v9, off offset:128
